# A-tile pairing (4 LDS stages) also in the w_in / w_o GEMM loops of phases 2 and 6
# baseline (speedup 1.0000x reference)
.LBB0_211:
	s_cmp_gt_u32 s85, 61
	s_cselect_b64 s[8:9], -1, 0
	s_and_b64 vcc, exec, s[8:9]
	s_cbranch_vccnz .LBB0_213
	s_lshl_b32 s2, s84, 14
	s_add_i32 s2, s2, s71
	s_mov_b32 s33, m0
	s_mov_b32 m0, s2
	s_nop 0
	global_load_lds_dwordx4 v[186:187], off
	s_mov_b32 m0, s33
	s_addk_i32 s2, 0x2000
	s_mov_b32 s33, m0
	s_mov_b32 m0, s2
	s_nop 0
	global_load_lds_dwordx4 v[184:185], off
	s_mov_b32 m0, s33
	s_bitcmp1_b32 s85, 0
	s_cbranch_scc1 .LBB0_213
	s_and_b32 s2, s85, 2
	s_cmp_eq_u32 s2, 0
	s_cselect_b32 s33, 0x8000, 0
	s_add_i32 s33, s33, s70
	s_mov_b32 s34, m0
	s_mov_b32 m0, s33
	s_nop 0
	global_load_lds_dwordx4 v[182:183], off
	s_mov_b32 m0, s34
	s_addk_i32 s33, 0x2000
	s_mov_b32 s34, m0
	s_mov_b32 m0, s33
	s_nop 0
	global_load_lds_dwordx4 v[180:181], off
	s_mov_b32 m0, s34
	s_cmp_eq_u32 s2, 0
	s_cselect_b32 s33, 0x14000, 0
	s_add_i32 s33, s33, s70
	s_addk_i32 s33, 0x3fc0
	s_mov_b32 s34, m0
	s_mov_b32 m0, s33
	s_nop 0
	global_load_lds_dwordx4 v[182:183], off offset:64
	s_mov_b32 m0, s34
	s_addk_i32 s33, 0x2000
	s_mov_b32 s34, m0
	s_mov_b32 m0, s33
	s_nop 0
	global_load_lds_dwordx4 v[180:181], off offset:64
	s_mov_b32 m0, s34
.LBB0_213:
	s_lshl_b32 s2, s86, 14
	s_add_i32 s33, s2, 0
	v_add_u32_e32 v132, s33, v178
	v_add_u32_e32 v136, s33, v189
	v_add_u32_e32 v140, s33, v190
	v_add_u32_e32 v144, s33, v191
	s_and_b32 s34, s85, 3
	s_lshl_b32 s34, s34, 14
	s_cmp_eq_u32 s34, 0xc000
	s_cselect_b32 s34, 0x18000, s34
	v_add_u32_e32 v146, s34, v188
	ds_read_b64_tr_b16 v[130:131], v132 offset:49152
	ds_read_b64_tr_b16 v[132:133], v132 offset:51200
	ds_read_b64_tr_b16 v[134:135], v136 offset:49152
	ds_read_b64_tr_b16 v[136:137], v136 offset:51200
	ds_read_b64_tr_b16 v[138:139], v140 offset:49152
	ds_read_b64_tr_b16 v[140:141], v140 offset:51200
	ds_read_b64_tr_b16 v[142:143], v144 offset:49152
	ds_read_b64_tr_b16 v[144:145], v144 offset:51200
	ds_read_b128 v[174:177], v146
	ds_read_b128 v[170:173], v146 offset:1024
	ds_read_b128 v[166:169], v146 offset:2048
	ds_read_b128 v[162:165], v146 offset:3072
	ds_read_b128 v[158:161], v146 offset:4096
	ds_read_b128 v[154:157], v146 offset:5120
	ds_read_b128 v[150:153], v146 offset:6144
	ds_read_b128 v[146:149], v146 offset:7168
	s_mov_b64 s[34:35], -1
	s_and_b64 vcc, exec, s[8:9]
	s_cbranch_vccz .LBB0_215
	s_waitcnt vmcnt(0) lgkmcnt(0)
	s_mov_b64 s[34:35], 0
.LBB0_215:
	s_andn2_b64 vcc, exec, s[34:35]
	s_cbranch_vccnz .LBB0_210
	s_bitcmp1_b32 s85, 0
	s_cbranch_scc1 .Lp2_wait_odd
	s_waitcnt vmcnt(6) lgkmcnt(0)
	s_branch .LBB0_210
.Lp2_wait_odd:
	s_waitcnt vmcnt(4) lgkmcnt(0)
	s_branch .LBB0_210

.LBB0_615:
	s_cmp_gt_u32 s61, 61
	s_cselect_b64 s[34:35], -1, 0
	s_and_b64 vcc, exec, s[34:35]
	s_cbranch_vccnz .LBB0_617
	s_lshl_b32 s2, s60, 14
	s_add_i32 s2, s2, s59
	s_mov_b32 s33, m0
	s_mov_b32 m0, s2
	s_nop 0
	global_load_lds_dwordx4 v[186:187], off
	s_mov_b32 m0, s33
	s_addk_i32 s2, 0x2000
	s_mov_b32 s33, m0
	s_mov_b32 m0, s2
	s_nop 0
	global_load_lds_dwordx4 v[184:185], off
	s_mov_b32 m0, s33
	s_bitcmp1_b32 s61, 0
	s_cbranch_scc1 .LBB0_617
	s_and_b32 s2, s61, 2
	s_cmp_eq_u32 s2, 0
	s_cselect_b32 s33, 0x8000, 0
	s_add_i32 s33, s33, s58
	s_mov_b32 s40, m0
	s_mov_b32 m0, s33
	s_nop 0
	global_load_lds_dwordx4 v[182:183], off
	s_mov_b32 m0, s40
	s_addk_i32 s33, 0x2000
	s_mov_b32 s40, m0
	s_mov_b32 m0, s33
	s_nop 0
	global_load_lds_dwordx4 v[180:181], off
	s_mov_b32 m0, s40
	s_cmp_eq_u32 s2, 0
	s_cselect_b32 s33, 0x14000, 0
	s_add_i32 s33, s33, s58
	s_addk_i32 s33, 0x3fc0
	s_mov_b32 s40, m0
	s_mov_b32 m0, s33
	s_nop 0
	global_load_lds_dwordx4 v[182:183], off offset:64
	s_mov_b32 m0, s40
	s_addk_i32 s33, 0x2000
	s_mov_b32 s40, m0
	s_mov_b32 m0, s33
	s_nop 0
	global_load_lds_dwordx4 v[180:181], off offset:64
	s_mov_b32 m0, s40
.LBB0_617:
	s_lshl_b32 s2, s62, 14
	s_add_i32 s33, s2, 0
	v_add_u32_e32 v1, s33, v178
	v_add_u32_e32 v136, s33, v189
	ds_read_b64_tr_b16 v[130:131], v1 offset:49152
	ds_read_b64_tr_b16 v[132:133], v1 offset:51200
	ds_read_b64_tr_b16 v[134:135], v136 offset:49152
	ds_read_b64_tr_b16 v[136:137], v136 offset:51200
	v_add_u32_e32 v1, s33, v190
	v_add_u32_e32 v144, s33, v191
	ds_read_b64_tr_b16 v[138:139], v1 offset:49152
	ds_read_b64_tr_b16 v[140:141], v1 offset:51200
	ds_read_b64_tr_b16 v[142:143], v144 offset:49152
	ds_read_b64_tr_b16 v[144:145], v144 offset:51200
	s_and_b32 s40, s61, 3
	s_lshl_b32 s40, s40, 14
	s_cmp_eq_u32 s40, 0xc000
	s_cselect_b32 s40, 0x18000, s40
	v_add_u32_e32 v1, s40, v188
	ds_read_b128 v[174:177], v1
	ds_read_b128 v[170:173], v1 offset:1024
	ds_read_b128 v[166:169], v1 offset:2048
	ds_read_b128 v[162:165], v1 offset:3072
	ds_read_b128 v[158:161], v1 offset:4096
	ds_read_b128 v[154:157], v1 offset:5120
	ds_read_b128 v[150:153], v1 offset:6144
	ds_read_b128 v[146:149], v1 offset:7168
	s_mov_b64 s[40:41], -1
	s_and_b64 vcc, exec, s[34:35]
	s_cbranch_vccz .LBB0_619
	s_waitcnt vmcnt(0) lgkmcnt(0)
	s_mov_b64 s[40:41], 0
.LBB0_619:
	s_andn2_b64 vcc, exec, s[40:41]
	s_cbranch_vccnz .LBB0_614
	s_bitcmp1_b32 s61, 0
	s_cbranch_scc1 .Lp6_wait_odd
	s_waitcnt vmcnt(6) lgkmcnt(0)
	s_branch .LBB0_614
